# code placement: the 14 GEMM K-loop back-edge targets aligned to 64 bytes (padding sits behind an unconditional branch, never executed)
# speedup vs baseline: 1.0082x; 1.0038x over previous
.LBB0_290:
	s_ashr_i32 s15, s14, 31
	s_lshl_b64 s[16:17], s[14:15], 19
	v_readlane_b32 s20, v254, 49
	v_readlane_b32 s21, v254, 50
	s_add_u32 s16, s20, s16
	s_addc_u32 s17, s21, s17
	s_and_b64 s[20:21], s[18:19], exec
	s_cselect_b32 s15, s17, s25
	s_cselect_b32 s23, s16, s24
	s_ashr_i32 s13, s12, 31
	s_lshl_b64 s[20:21], s[12:13], 19
	s_add_u32 s20, s4, s20
	s_addc_u32 s21, s5, s21
	s_and_b64 s[34:35], s[18:19], exec
	s_cselect_b32 s13, s21, s29
	s_cselect_b32 s60, s20, s28
	s_cmp_eq_u32 s30, 0
	s_cselect_b32 s61, -2, 0
	s_add_u32 s63, s28, 0x10000
	s_mov_b32 s62, 0
	s_addc_u32 s64, s29, 0
	v_lshl_add_u64 v[210:211], s[24:25], 0, v[204:205]
	v_lshl_add_u64 v[212:213], s[24:25], 0, v[206:207]
	v_mov_b64_e32 v[2:3], 0
	v_mov_b64_e32 v[4:5], 0
	v_mov_b64_e32 v[6:7], 0
	v_mov_b64_e32 v[8:9], 0
	v_mov_b64_e32 v[10:11], 0
	v_mov_b64_e32 v[12:13], 0
	v_mov_b64_e32 v[14:15], 0
	v_mov_b64_e32 v[16:17], 0
	v_mov_b64_e32 v[18:19], 0
	v_mov_b64_e32 v[20:21], 0
	v_mov_b64_e32 v[22:23], 0
	v_mov_b64_e32 v[24:25], 0
	v_mov_b64_e32 v[26:27], 0
	v_mov_b64_e32 v[28:29], 0
	v_mov_b64_e32 v[30:31], 0
	v_mov_b64_e32 v[32:33], 0
	v_mov_b64_e32 v[34:35], 0
	v_mov_b64_e32 v[36:37], 0
	v_mov_b64_e32 v[38:39], 0
	v_mov_b64_e32 v[40:41], 0
	v_mov_b64_e32 v[42:43], 0
	v_mov_b64_e32 v[44:45], 0
	v_mov_b64_e32 v[46:47], 0
	v_mov_b64_e32 v[48:49], 0
	v_mov_b64_e32 v[50:51], 0
	v_mov_b64_e32 v[52:53], 0
	v_mov_b64_e32 v[54:55], 0
	v_mov_b64_e32 v[56:57], 0
	v_mov_b64_e32 v[58:59], 0
	v_mov_b64_e32 v[60:61], 0
	v_mov_b64_e32 v[62:63], 0
	v_mov_b64_e32 v[64:65], 0
	v_mov_b64_e32 v[66:67], 0
	v_mov_b64_e32 v[68:69], 0
	v_mov_b64_e32 v[70:71], 0
	v_mov_b64_e32 v[72:73], 0
	v_mov_b64_e32 v[74:75], 0
	v_mov_b64_e32 v[76:77], 0
	v_mov_b64_e32 v[78:79], 0
	v_mov_b64_e32 v[80:81], 0
	v_mov_b64_e32 v[82:83], 0
	v_mov_b64_e32 v[84:85], 0
	v_mov_b64_e32 v[86:87], 0
	v_mov_b64_e32 v[88:89], 0
	v_mov_b64_e32 v[90:91], 0
	v_mov_b64_e32 v[92:93], 0
	v_mov_b64_e32 v[94:95], 0
	v_mov_b64_e32 v[96:97], 0
	v_mov_b64_e32 v[98:99], 0
	v_mov_b64_e32 v[100:101], 0
	v_mov_b64_e32 v[102:103], 0
	v_mov_b64_e32 v[104:105], 0
	v_mov_b64_e32 v[106:107], 0
	v_mov_b64_e32 v[108:109], 0
	v_mov_b64_e32 v[110:111], 0
	v_mov_b64_e32 v[112:113], 0
	v_mov_b64_e32 v[114:115], 0
	v_mov_b64_e32 v[116:117], 0
	v_mov_b64_e32 v[118:119], 0
	v_mov_b64_e32 v[120:121], 0
	v_mov_b64_e32 v[122:123], 0
	v_mov_b64_e32 v[124:125], 0
	v_mov_b64_e32 v[126:127], 0
	v_mov_b64_e32 v[128:129], 0
	s_waitcnt lgkmcnt(0)
	s_branch .LBB0_292
	.p2align	6

.LBB0_591:
	s_ashr_i32 s15, s14, 31
	s_lshl_b64 s[16:17], s[14:15], 19
	v_readlane_b32 s20, v254, 49
	v_readlane_b32 s21, v254, 50
	s_add_u32 s16, s20, s16
	s_addc_u32 s17, s21, s17
	s_and_b64 s[20:21], s[18:19], exec
	s_cselect_b32 s15, s17, s27
	s_cselect_b32 s25, s16, s26
	s_ashr_i32 s13, s12, 31
	s_lshl_b64 s[20:21], s[12:13], 19
	s_add_u32 s20, s4, s20
	s_addc_u32 s21, s5, s21
	s_and_b64 s[36:37], s[18:19], exec
	s_cselect_b32 s13, s21, s31
	s_cselect_b32 s60, s20, s30
	s_cmp_eq_u32 s34, 0
	s_cselect_b32 s61, -2, 0
	s_add_u32 s63, s30, 0x10000
	s_mov_b32 s62, 0
	s_addc_u32 s64, s31, 0
	v_lshl_add_u64 v[210:211], s[26:27], 0, v[204:205]
	v_lshl_add_u64 v[212:213], s[26:27], 0, v[206:207]
	v_mov_b64_e32 v[2:3], 0
	v_mov_b64_e32 v[4:5], 0
	v_mov_b64_e32 v[6:7], 0
	v_mov_b64_e32 v[8:9], 0
	v_mov_b64_e32 v[10:11], 0
	v_mov_b64_e32 v[12:13], 0
	v_mov_b64_e32 v[14:15], 0
	v_mov_b64_e32 v[16:17], 0
	v_mov_b64_e32 v[18:19], 0
	v_mov_b64_e32 v[20:21], 0
	v_mov_b64_e32 v[22:23], 0
	v_mov_b64_e32 v[24:25], 0
	v_mov_b64_e32 v[26:27], 0
	v_mov_b64_e32 v[28:29], 0
	v_mov_b64_e32 v[30:31], 0
	v_mov_b64_e32 v[32:33], 0
	v_mov_b64_e32 v[34:35], 0
	v_mov_b64_e32 v[36:37], 0
	v_mov_b64_e32 v[38:39], 0
	v_mov_b64_e32 v[40:41], 0
	v_mov_b64_e32 v[42:43], 0
	v_mov_b64_e32 v[44:45], 0
	v_mov_b64_e32 v[46:47], 0
	v_mov_b64_e32 v[48:49], 0
	v_mov_b64_e32 v[50:51], 0
	v_mov_b64_e32 v[52:53], 0
	v_mov_b64_e32 v[54:55], 0
	v_mov_b64_e32 v[56:57], 0
	v_mov_b64_e32 v[58:59], 0
	v_mov_b64_e32 v[60:61], 0
	v_mov_b64_e32 v[62:63], 0
	v_mov_b64_e32 v[64:65], 0
	v_mov_b64_e32 v[66:67], 0
	v_mov_b64_e32 v[68:69], 0
	v_mov_b64_e32 v[70:71], 0
	v_mov_b64_e32 v[72:73], 0
	v_mov_b64_e32 v[74:75], 0
	v_mov_b64_e32 v[76:77], 0
	v_mov_b64_e32 v[78:79], 0
	v_mov_b64_e32 v[80:81], 0
	v_mov_b64_e32 v[82:83], 0
	v_mov_b64_e32 v[84:85], 0
	v_mov_b64_e32 v[86:87], 0
	v_mov_b64_e32 v[88:89], 0
	v_mov_b64_e32 v[90:91], 0
	v_mov_b64_e32 v[92:93], 0
	v_mov_b64_e32 v[94:95], 0
	v_mov_b64_e32 v[96:97], 0
	v_mov_b64_e32 v[98:99], 0
	v_mov_b64_e32 v[100:101], 0
	v_mov_b64_e32 v[102:103], 0
	v_mov_b64_e32 v[104:105], 0
	v_mov_b64_e32 v[106:107], 0
	v_mov_b64_e32 v[108:109], 0
	v_mov_b64_e32 v[110:111], 0
	v_mov_b64_e32 v[112:113], 0
	v_mov_b64_e32 v[114:115], 0
	v_mov_b64_e32 v[116:117], 0
	v_mov_b64_e32 v[118:119], 0
	v_mov_b64_e32 v[120:121], 0
	v_mov_b64_e32 v[122:123], 0
	v_mov_b64_e32 v[124:125], 0
	v_mov_b64_e32 v[126:127], 0
	v_mov_b64_e32 v[128:129], 0
	s_branch .LBB0_593
	.p2align	6

.LBB0_749:
	s_add_i32 s51, s28, 1
	s_cmp_lt_u32 s51, s45
	s_cselect_b64 s[4:5], -1, 0
	s_and_b64 s[26:27], s[4:5], s[0:1]
	s_ashr_i32 s15, s14, 31
	s_andn2_b64 vcc, exec, s[26:27]
	s_lshl_b64 s[16:17], s[14:15], 20
	s_add_u32 s16, s33, s16
	s_addc_u32 s17, s42, s17
	s_and_b64 s[18:19], s[26:27], exec
	s_cselect_b32 s15, s17, s23
	s_cselect_b32 s52, s16, s22
	s_ashr_i32 s13, s12, 31
	s_lshl_b64 s[18:19], s[12:13], 20
	s_add_u32 s18, s6, s18
	s_addc_u32 s19, s7, s19
	v_cndmask_b32_e64 v2, 0, 1, s[26:27]
	s_and_b64 s[26:27], s[26:27], exec
	s_cselect_b32 s13, s19, s25
	s_cselect_b32 s53, s18, s24
	s_cmp_eq_u32 s28, 0
	v_cmp_ne_u32_e64 s[4:5], 1, v2
	s_cselect_b32 s54, -2, 0
	s_add_u32 s56, s24, 0x10000
	v_mov_b32_e32 v2, 0
	s_mov_b32 s55, 0
	s_addc_u32 s57, s25, 0
	v_lshl_add_u64 v[206:207], s[22:23], 0, v[202:203]
	v_lshl_add_u64 v[208:209], s[22:23], 0, v[204:205]
	s_mov_b64 s[24:25], 0
	v_mov_b32_e32 v3, 0
	v_mov_b64_e32 v[4:5], 0
	v_mov_b64_e32 v[6:7], 0
	v_mov_b64_e32 v[8:9], 0
	v_mov_b64_e32 v[10:11], 0
	v_mov_b64_e32 v[12:13], 0
	v_mov_b64_e32 v[14:15], 0
	v_mov_b64_e32 v[16:17], 0
	v_mov_b64_e32 v[18:19], 0
	v_mov_b64_e32 v[20:21], 0
	v_mov_b64_e32 v[22:23], 0
	v_mov_b64_e32 v[24:25], 0
	v_mov_b64_e32 v[26:27], 0
	v_mov_b64_e32 v[28:29], 0
	v_mov_b64_e32 v[30:31], 0
	v_mov_b64_e32 v[32:33], 0
	v_mov_b64_e32 v[34:35], 0
	v_mov_b64_e32 v[36:37], 0
	v_mov_b64_e32 v[38:39], 0
	v_mov_b64_e32 v[40:41], 0
	v_mov_b64_e32 v[42:43], 0
	v_mov_b64_e32 v[44:45], 0
	v_mov_b64_e32 v[46:47], 0
	v_mov_b64_e32 v[48:49], 0
	v_mov_b64_e32 v[50:51], 0
	v_mov_b64_e32 v[52:53], 0
	v_mov_b64_e32 v[54:55], 0
	v_mov_b64_e32 v[56:57], 0
	v_mov_b64_e32 v[58:59], 0
	v_mov_b64_e32 v[60:61], 0
	v_mov_b64_e32 v[62:63], 0
	v_mov_b64_e32 v[64:65], 0
	v_mov_b64_e32 v[82:83], 0
	v_mov_b64_e32 v[84:85], 0
	v_mov_b64_e32 v[86:87], 0
	v_mov_b64_e32 v[88:89], 0
	v_mov_b64_e32 v[90:91], 0
	v_mov_b64_e32 v[92:93], 0
	v_mov_b64_e32 v[94:95], 0
	v_mov_b64_e32 v[96:97], 0
	v_mov_b64_e32 v[98:99], 0
	v_mov_b64_e32 v[100:101], 0
	v_mov_b64_e32 v[102:103], 0
	v_mov_b64_e32 v[104:105], 0
	v_mov_b64_e32 v[106:107], 0
	v_mov_b64_e32 v[108:109], 0
	v_mov_b64_e32 v[110:111], 0
	v_mov_b64_e32 v[112:113], 0
	v_mov_b64_e32 v[114:115], 0
	v_mov_b64_e32 v[116:117], 0
	v_mov_b64_e32 v[118:119], 0
	v_mov_b64_e32 v[120:121], 0
	v_mov_b64_e32 v[122:123], 0
	v_mov_b64_e32 v[124:125], 0
	v_mov_b64_e32 v[126:127], 0
	v_mov_b64_e32 v[128:129], 0
	v_mov_b64_e32 v[130:131], 0
	v_mov_b64_e32 v[132:133], 0
	v_mov_b64_e32 v[134:135], 0
	v_mov_b64_e32 v[136:137], 0
	v_mov_b64_e32 v[138:139], 0
	v_mov_b64_e32 v[140:141], 0
	v_mov_b64_e32 v[142:143], 0
	v_mov_b64_e32 v[144:145], 0
	s_waitcnt lgkmcnt(0)
	s_branch .LBB0_751
	.p2align	6

.LBB0_1050:
	s_ashr_i32 s11, s10, 31
	s_lshl_b64 s[12:13], s[10:11], 20
	s_add_u32 s12, s33, s12
	s_addc_u32 s13, s42, s13
	s_and_b64 s[16:17], s[14:15], exec
	s_cselect_b32 s11, s13, s23
	s_cselect_b32 s19, s12, s22
	s_ashr_i32 s9, s8, 31
	s_lshl_b64 s[16:17], s[8:9], 20
	s_add_u32 s16, s6, s16
	s_addc_u32 s17, s7, s17
	s_and_b64 s[30:31], s[14:15], exec
	s_cselect_b32 s9, s17, s27
	s_cselect_b32 s53, s16, s26
	s_cmp_eq_u32 s28, 0
	s_cselect_b32 s54, -2, 0
	s_add_u32 s56, s26, 0x10000
	v_mov_b32_e32 v2, 0
	s_mov_b32 s55, 0
	s_addc_u32 s57, s27, 0
	v_lshl_add_u64 v[208:209], s[22:23], 0, v[202:203]
	v_lshl_add_u64 v[210:211], s[22:23], 0, v[204:205]
	v_mov_b32_e32 v3, 0
	v_mov_b64_e32 v[4:5], 0
	v_mov_b64_e32 v[6:7], 0
	v_mov_b64_e32 v[8:9], 0
	v_mov_b64_e32 v[10:11], 0
	v_mov_b64_e32 v[12:13], 0
	v_mov_b64_e32 v[14:15], 0
	v_mov_b64_e32 v[16:17], 0
	v_mov_b64_e32 v[18:19], 0
	v_mov_b64_e32 v[20:21], 0
	v_mov_b64_e32 v[22:23], 0
	v_mov_b64_e32 v[24:25], 0
	v_mov_b64_e32 v[26:27], 0
	v_mov_b64_e32 v[28:29], 0
	v_mov_b64_e32 v[30:31], 0
	v_mov_b64_e32 v[32:33], 0
	v_mov_b64_e32 v[34:35], 0
	v_mov_b64_e32 v[36:37], 0
	v_mov_b64_e32 v[38:39], 0
	v_mov_b64_e32 v[40:41], 0
	v_mov_b64_e32 v[42:43], 0
	v_mov_b64_e32 v[44:45], 0
	v_mov_b64_e32 v[46:47], 0
	v_mov_b64_e32 v[48:49], 0
	v_mov_b64_e32 v[50:51], 0
	v_mov_b64_e32 v[52:53], 0
	v_mov_b64_e32 v[54:55], 0
	v_mov_b64_e32 v[56:57], 0
	v_mov_b64_e32 v[58:59], 0
	v_mov_b64_e32 v[60:61], 0
	v_mov_b64_e32 v[62:63], 0
	v_mov_b64_e32 v[64:65], 0
	v_mov_b64_e32 v[82:83], 0
	v_mov_b64_e32 v[84:85], 0
	v_mov_b64_e32 v[86:87], 0
	v_mov_b64_e32 v[88:89], 0
	v_mov_b64_e32 v[90:91], 0
	v_mov_b64_e32 v[92:93], 0
	v_mov_b64_e32 v[94:95], 0
	v_mov_b64_e32 v[96:97], 0
	v_mov_b64_e32 v[98:99], 0
	v_mov_b64_e32 v[100:101], 0
	v_mov_b64_e32 v[102:103], 0
	v_mov_b64_e32 v[104:105], 0
	v_mov_b64_e32 v[106:107], 0
	v_mov_b64_e32 v[108:109], 0
	v_mov_b64_e32 v[110:111], 0
	v_mov_b64_e32 v[112:113], 0
	v_mov_b64_e32 v[114:115], 0
	v_mov_b64_e32 v[116:117], 0
	v_mov_b64_e32 v[118:119], 0
	v_mov_b64_e32 v[120:121], 0
	v_mov_b64_e32 v[122:123], 0
	v_mov_b64_e32 v[124:125], 0
	v_mov_b64_e32 v[126:127], 0
	v_mov_b64_e32 v[128:129], 0
	v_mov_b64_e32 v[130:131], 0
	v_mov_b64_e32 v[132:133], 0
	v_mov_b64_e32 v[134:135], 0
	v_mov_b64_e32 v[136:137], 0
	v_mov_b64_e32 v[138:139], 0
	v_mov_b64_e32 v[140:141], 0
	v_mov_b64_e32 v[142:143], 0
	v_mov_b64_e32 v[144:145], 0
	s_branch .LBB0_1052
	.p2align	6

.LBB0_1183:
	s_ashr_i32 s11, s10, 31
	s_lshl_b64 s[12:13], s[10:11], 19
	v_readlane_b32 s16, v254, 49
	v_readlane_b32 s17, v254, 50
	s_add_u32 s12, s16, s12
	s_addc_u32 s13, s17, s13
	s_and_b64 s[16:17], s[14:15], exec
	s_cselect_b32 s11, s13, s21
	s_cselect_b32 s56, s12, s20
	s_ashr_i32 s9, s8, 31
	s_lshl_b64 s[16:17], s[8:9], 19
	s_add_u32 s16, s6, s16
	s_addc_u32 s17, s7, s17
	s_and_b64 s[28:29], s[14:15], exec
	s_cselect_b32 s9, s17, s25
	s_cselect_b32 s57, s16, s24
	s_cmp_eq_u32 s26, 0
	s_cselect_b32 s58, -2, 0
	s_add_u32 s60, s24, 0x10000
	s_mov_b32 s59, 0
	s_addc_u32 s61, s25, 0
	v_lshl_add_u64 v[236:237], s[20:21], 0, v[232:233]
	v_lshl_add_u64 v[238:239], s[20:21], 0, v[234:235]
	v_mov_b64_e32 v[2:3], 0
	v_mov_b64_e32 v[4:5], 0
	v_mov_b64_e32 v[6:7], 0
	v_mov_b64_e32 v[8:9], 0
	v_mov_b64_e32 v[10:11], 0
	v_mov_b64_e32 v[12:13], 0
	v_mov_b64_e32 v[14:15], 0
	v_mov_b64_e32 v[16:17], 0
	v_mov_b64_e32 v[18:19], 0
	v_mov_b64_e32 v[20:21], 0
	v_mov_b64_e32 v[22:23], 0
	v_mov_b64_e32 v[24:25], 0
	v_mov_b64_e32 v[26:27], 0
	v_mov_b64_e32 v[28:29], 0
	v_mov_b64_e32 v[30:31], 0
	v_mov_b64_e32 v[32:33], 0
	v_mov_b64_e32 v[34:35], 0
	v_mov_b64_e32 v[36:37], 0
	v_mov_b64_e32 v[38:39], 0
	v_mov_b64_e32 v[40:41], 0
	v_mov_b64_e32 v[42:43], 0
	v_mov_b64_e32 v[44:45], 0
	v_mov_b64_e32 v[46:47], 0
	v_mov_b64_e32 v[48:49], 0
	v_mov_b64_e32 v[50:51], 0
	v_mov_b64_e32 v[52:53], 0
	v_mov_b64_e32 v[54:55], 0
	v_mov_b64_e32 v[56:57], 0
	v_mov_b64_e32 v[58:59], 0
	v_mov_b64_e32 v[60:61], 0
	v_mov_b64_e32 v[62:63], 0
	v_mov_b64_e32 v[64:65], 0
	v_mov_b64_e32 v[66:67], 0
	v_mov_b64_e32 v[68:69], 0
	v_mov_b64_e32 v[70:71], 0
	v_mov_b64_e32 v[72:73], 0
	v_mov_b64_e32 v[74:75], 0
	v_mov_b64_e32 v[76:77], 0
	v_mov_b64_e32 v[78:79], 0
	v_mov_b64_e32 v[80:81], 0
	v_mov_b64_e32 v[82:83], 0
	v_mov_b64_e32 v[84:85], 0
	v_mov_b64_e32 v[86:87], 0
	v_mov_b64_e32 v[88:89], 0
	v_mov_b64_e32 v[90:91], 0
	v_mov_b64_e32 v[92:93], 0
	v_mov_b64_e32 v[94:95], 0
	v_mov_b64_e32 v[96:97], 0
	v_mov_b64_e32 v[98:99], 0
	v_mov_b64_e32 v[100:101], 0
	v_mov_b64_e32 v[102:103], 0
	v_mov_b64_e32 v[104:105], 0
	v_mov_b64_e32 v[106:107], 0
	v_mov_b64_e32 v[108:109], 0
	v_mov_b64_e32 v[110:111], 0
	v_mov_b64_e32 v[112:113], 0
	v_mov_b64_e32 v[114:115], 0
	v_mov_b64_e32 v[116:117], 0
	v_mov_b64_e32 v[118:119], 0
	v_mov_b64_e32 v[120:121], 0
	v_mov_b64_e32 v[122:123], 0
	v_mov_b64_e32 v[124:125], 0
	v_mov_b64_e32 v[126:127], 0
	v_mov_b64_e32 v[128:129], 0
	s_waitcnt lgkmcnt(0)
	s_branch .LBB0_1185
	.p2align	6

.LBB0_1503:
	s_ashr_i32 s11, s10, 31
	s_lshl_b64 s[12:13], s[10:11], 19
	v_readlane_b32 s16, v254, 49
	v_readlane_b32 s17, v254, 50
	s_add_u32 s12, s16, s12
	s_addc_u32 s13, s17, s13
	s_and_b64 s[16:17], s[14:15], exec
	s_cselect_b32 s11, s13, s23
	s_cselect_b32 s19, s12, s22
	s_ashr_i32 s9, s8, 31
	s_lshl_b64 s[16:17], s[8:9], 19
	s_add_u32 s16, s6, s16
	s_addc_u32 s17, s7, s17
	s_and_b64 s[30:31], s[14:15], exec
	s_cselect_b32 s9, s17, s27
	s_cselect_b32 s21, s16, s26
	s_cmp_eq_u32 s28, 0
	s_cselect_b32 s58, -2, 0
	s_add_u32 s60, s26, 0x10000
	s_mov_b32 s59, 0
	s_addc_u32 s61, s27, 0
	v_lshl_add_u64 v[238:239], s[22:23], 0, v[232:233]
	v_lshl_add_u64 v[240:241], s[22:23], 0, v[234:235]
	v_mov_b64_e32 v[2:3], 0
	v_mov_b64_e32 v[4:5], 0
	v_mov_b64_e32 v[6:7], 0
	v_mov_b64_e32 v[8:9], 0
	v_mov_b64_e32 v[10:11], 0
	v_mov_b64_e32 v[12:13], 0
	v_mov_b64_e32 v[14:15], 0
	v_mov_b64_e32 v[16:17], 0
	v_mov_b64_e32 v[18:19], 0
	v_mov_b64_e32 v[20:21], 0
	v_mov_b64_e32 v[22:23], 0
	v_mov_b64_e32 v[24:25], 0
	v_mov_b64_e32 v[26:27], 0
	v_mov_b64_e32 v[28:29], 0
	v_mov_b64_e32 v[30:31], 0
	v_mov_b64_e32 v[32:33], 0
	v_mov_b64_e32 v[34:35], 0
	v_mov_b64_e32 v[36:37], 0
	v_mov_b64_e32 v[38:39], 0
	v_mov_b64_e32 v[40:41], 0
	v_mov_b64_e32 v[42:43], 0
	v_mov_b64_e32 v[44:45], 0
	v_mov_b64_e32 v[46:47], 0
	v_mov_b64_e32 v[48:49], 0
	v_mov_b64_e32 v[50:51], 0
	v_mov_b64_e32 v[52:53], 0
	v_mov_b64_e32 v[54:55], 0
	v_mov_b64_e32 v[56:57], 0
	v_mov_b64_e32 v[58:59], 0
	v_mov_b64_e32 v[60:61], 0
	v_mov_b64_e32 v[62:63], 0
	v_mov_b64_e32 v[64:65], 0
	v_mov_b64_e32 v[66:67], 0
	v_mov_b64_e32 v[68:69], 0
	v_mov_b64_e32 v[70:71], 0
	v_mov_b64_e32 v[72:73], 0
	v_mov_b64_e32 v[74:75], 0
	v_mov_b64_e32 v[76:77], 0
	v_mov_b64_e32 v[78:79], 0
	v_mov_b64_e32 v[80:81], 0
	v_mov_b64_e32 v[82:83], 0
	v_mov_b64_e32 v[84:85], 0
	v_mov_b64_e32 v[86:87], 0
	v_mov_b64_e32 v[88:89], 0
	v_mov_b64_e32 v[90:91], 0
	v_mov_b64_e32 v[92:93], 0
	v_mov_b64_e32 v[94:95], 0
	v_mov_b64_e32 v[96:97], 0
	v_mov_b64_e32 v[98:99], 0
	v_mov_b64_e32 v[100:101], 0
	v_mov_b64_e32 v[102:103], 0
	v_mov_b64_e32 v[104:105], 0
	v_mov_b64_e32 v[106:107], 0
	v_mov_b64_e32 v[108:109], 0
	v_mov_b64_e32 v[110:111], 0
	v_mov_b64_e32 v[112:113], 0
	v_mov_b64_e32 v[114:115], 0
	v_mov_b64_e32 v[116:117], 0
	v_mov_b64_e32 v[118:119], 0
	v_mov_b64_e32 v[120:121], 0
	v_mov_b64_e32 v[122:123], 0
	v_mov_b64_e32 v[124:125], 0
	v_mov_b64_e32 v[126:127], 0
	v_mov_b64_e32 v[128:129], 0
	s_branch .LBB0_1505
	.p2align	6

.LBB0_1586:
	s_cmp_eq_u32 s20, 0
	s_cselect_b32 s49, -2, 0
	s_add_u32 s51, s18, 0x10000
	v_mov_b32_e32 v66, 0
	s_mov_b32 s50, 0
	s_addc_u32 s52, s19, 0
	v_lshl_add_u64 v[206:207], s[16:17], 0, v[202:203]
	v_lshl_add_u64 v[208:209], s[16:17], 0, v[204:205]
	s_mov_b64 s[18:19], 0
	v_mov_b32_e32 v67, 0
	v_mov_b64_e32 v[68:69], 0
	v_mov_b64_e32 v[70:71], 0
	v_mov_b64_e32 v[72:73], 0
	v_mov_b64_e32 v[74:75], 0
	v_mov_b64_e32 v[76:77], 0
	s_waitcnt lgkmcnt(0)
	v_mov_b64_e32 v[78:79], 0
	v_mov_b64_e32 v[80:81], 0
	v_mov_b64_e32 v[82:83], 0
	v_mov_b64_e32 v[84:85], 0
	v_mov_b64_e32 v[86:87], 0
	v_mov_b64_e32 v[88:89], 0
	v_mov_b64_e32 v[90:91], 0
	v_mov_b64_e32 v[92:93], 0
	v_mov_b64_e32 v[94:95], 0
	v_mov_b64_e32 v[96:97], 0
	v_mov_b64_e32 v[98:99], 0
	v_mov_b64_e32 v[100:101], 0
	v_mov_b64_e32 v[102:103], 0
	v_mov_b64_e32 v[104:105], 0
	v_mov_b64_e32 v[106:107], 0
	v_mov_b64_e32 v[108:109], 0
	v_mov_b64_e32 v[110:111], 0
	v_mov_b64_e32 v[112:113], 0
	v_mov_b64_e32 v[114:115], 0
	v_mov_b64_e32 v[116:117], 0
	v_mov_b64_e32 v[118:119], 0
	v_mov_b64_e32 v[120:121], 0
	v_mov_b64_e32 v[122:123], 0
	v_mov_b64_e32 v[124:125], 0
	v_mov_b64_e32 v[126:127], 0
	v_mov_b64_e32 v[128:129], 0
	v_mov_b64_e32 v[130:131], 0
	v_mov_b64_e32 v[132:133], 0
	v_mov_b64_e32 v[134:135], 0
	v_mov_b64_e32 v[136:137], 0
	v_mov_b64_e32 v[138:139], 0
	v_mov_b64_e32 v[140:141], 0
	v_mov_b64_e32 v[142:143], 0
	v_mov_b64_e32 v[144:145], 0
	v_mov_b64_e32 v[146:147], 0
	v_mov_b64_e32 v[148:149], 0
	v_mov_b64_e32 v[150:151], 0
	v_mov_b64_e32 v[152:153], 0
	v_mov_b64_e32 v[154:155], 0
	v_mov_b64_e32 v[156:157], 0
	v_mov_b64_e32 v[158:159], 0
	v_mov_b64_e32 v[160:161], 0
	v_mov_b64_e32 v[162:163], 0
	v_mov_b64_e32 v[164:165], 0
	v_mov_b64_e32 v[166:167], 0
	v_mov_b64_e32 v[168:169], 0
	v_mov_b64_e32 v[170:171], 0
	v_mov_b64_e32 v[172:173], 0
	v_mov_b64_e32 v[174:175], 0
	v_mov_b64_e32 v[176:177], 0
	v_mov_b64_e32 v[178:179], 0
	v_mov_b64_e32 v[180:181], 0
	v_mov_b64_e32 v[182:183], 0
	v_mov_b64_e32 v[184:185], 0
	v_mov_b64_e32 v[186:187], 0
	v_mov_b64_e32 v[188:189], 0
	v_mov_b64_e32 v[190:191], 0
	v_mov_b64_e32 v[192:193], 0
	s_branch .LBB0_1588
	.p2align	6

.LBB0_1939:
	s_cmp_eq_u32 s18, 0
	s_cselect_b32 s49, -2, 0
	s_add_u32 s51, s16, 0x10000
	v_mov_b32_e32 v66, 0
	s_mov_b32 s50, 0
	s_addc_u32 s52, s17, 0
	v_lshl_add_u64 v[208:209], s[14:15], 0, v[202:203]
	v_lshl_add_u64 v[210:211], s[14:15], 0, v[204:205]
	s_mov_b64 s[16:17], 0
	v_mov_b32_e32 v67, 0
	v_mov_b64_e32 v[68:69], 0
	v_mov_b64_e32 v[70:71], 0
	v_mov_b64_e32 v[72:73], 0
	v_mov_b64_e32 v[74:75], 0
	v_mov_b64_e32 v[76:77], 0
	v_mov_b64_e32 v[78:79], 0
	v_mov_b64_e32 v[80:81], 0
	v_mov_b64_e32 v[82:83], 0
	v_mov_b64_e32 v[84:85], 0
	v_mov_b64_e32 v[86:87], 0
	v_mov_b64_e32 v[88:89], 0
	v_mov_b64_e32 v[90:91], 0
	v_mov_b64_e32 v[92:93], 0
	v_mov_b64_e32 v[94:95], 0
	v_mov_b64_e32 v[96:97], 0
	v_mov_b64_e32 v[98:99], 0
	v_mov_b64_e32 v[100:101], 0
	v_mov_b64_e32 v[102:103], 0
	v_mov_b64_e32 v[104:105], 0
	v_mov_b64_e32 v[106:107], 0
	v_mov_b64_e32 v[108:109], 0
	v_mov_b64_e32 v[110:111], 0
	v_mov_b64_e32 v[112:113], 0
	v_mov_b64_e32 v[114:115], 0
	v_mov_b64_e32 v[116:117], 0
	v_mov_b64_e32 v[118:119], 0
	v_mov_b64_e32 v[120:121], 0
	v_mov_b64_e32 v[122:123], 0
	v_mov_b64_e32 v[124:125], 0
	v_mov_b64_e32 v[126:127], 0
	v_mov_b64_e32 v[128:129], 0
	v_mov_b64_e32 v[130:131], 0
	v_mov_b64_e32 v[132:133], 0
	v_mov_b64_e32 v[134:135], 0
	v_mov_b64_e32 v[136:137], 0
	v_mov_b64_e32 v[138:139], 0
	v_mov_b64_e32 v[140:141], 0
	v_mov_b64_e32 v[142:143], 0
	v_mov_b64_e32 v[144:145], 0
	v_mov_b64_e32 v[146:147], 0
	v_mov_b64_e32 v[148:149], 0
	v_mov_b64_e32 v[150:151], 0
	v_mov_b64_e32 v[152:153], 0
	v_mov_b64_e32 v[154:155], 0
	v_mov_b64_e32 v[156:157], 0
	v_mov_b64_e32 v[158:159], 0
	v_mov_b64_e32 v[160:161], 0
	v_mov_b64_e32 v[162:163], 0
	v_mov_b64_e32 v[164:165], 0
	v_mov_b64_e32 v[166:167], 0
	v_mov_b64_e32 v[168:169], 0
	v_mov_b64_e32 v[170:171], 0
	v_mov_b64_e32 v[172:173], 0
	v_mov_b64_e32 v[174:175], 0
	v_mov_b64_e32 v[176:177], 0
	v_mov_b64_e32 v[178:179], 0
	v_mov_b64_e32 v[180:181], 0
	v_mov_b64_e32 v[182:183], 0
	v_mov_b64_e32 v[184:185], 0
	v_mov_b64_e32 v[186:187], 0
	v_mov_b64_e32 v[188:189], 0
	v_mov_b64_e32 v[190:191], 0
	v_mov_b64_e32 v[192:193], 0
	s_branch .LBB0_1941
	.p2align	6

.LBB0_2077:
	s_ashr_i32 s21, s20, 31
	s_lshl_b64 s[22:23], s[20:21], 19
	v_readlane_b32 s26, v254, 49
	v_readlane_b32 s27, v254, 50
	s_add_u32 s22, s26, s22
	s_addc_u32 s23, s27, s23
	s_and_b64 s[26:27], s[24:25], exec
	s_cselect_b32 s2, s23, s1
	s_cselect_b32 s21, s22, s0
	s_ashr_i32 s19, s18, 31
	s_lshl_b64 s[26:27], s[18:19], 19
	s_add_u32 s26, s4, s26
	s_addc_u32 s27, s5, s27
	s_and_b64 s[40:41], s[24:25], exec
	s_cselect_b32 s19, s27, s37
	s_cselect_b32 s66, s26, s36
	s_cmp_eq_u32 s38, 0
	s_cselect_b32 s67, -2, 0
	s_add_u32 s69, s36, 0x10000
	s_mov_b32 s68, 0
	s_addc_u32 s70, s37, 0
	v_lshl_add_u64 v[210:211], s[0:1], 0, v[204:205]
	v_lshl_add_u64 v[212:213], s[0:1], 0, v[206:207]
	v_mov_b64_e32 v[2:3], 0
	v_mov_b64_e32 v[4:5], 0
	v_mov_b64_e32 v[6:7], 0
	v_mov_b64_e32 v[8:9], 0
	v_mov_b64_e32 v[10:11], 0
	v_mov_b64_e32 v[12:13], 0
	v_mov_b64_e32 v[14:15], 0
	v_mov_b64_e32 v[16:17], 0
	v_mov_b64_e32 v[18:19], 0
	v_mov_b64_e32 v[20:21], 0
	v_mov_b64_e32 v[22:23], 0
	v_mov_b64_e32 v[24:25], 0
	v_mov_b64_e32 v[26:27], 0
	v_mov_b64_e32 v[28:29], 0
	v_mov_b64_e32 v[30:31], 0
	v_mov_b64_e32 v[32:33], 0
	v_mov_b64_e32 v[34:35], 0
	v_mov_b64_e32 v[36:37], 0
	v_mov_b64_e32 v[38:39], 0
	v_mov_b64_e32 v[40:41], 0
	v_mov_b64_e32 v[42:43], 0
	v_mov_b64_e32 v[44:45], 0
	v_mov_b64_e32 v[46:47], 0
	v_mov_b64_e32 v[48:49], 0
	v_mov_b64_e32 v[50:51], 0
	v_mov_b64_e32 v[52:53], 0
	v_mov_b64_e32 v[54:55], 0
	v_mov_b64_e32 v[56:57], 0
	v_mov_b64_e32 v[58:59], 0
	v_mov_b64_e32 v[60:61], 0
	v_mov_b64_e32 v[62:63], 0
	v_mov_b64_e32 v[64:65], 0
	v_mov_b64_e32 v[66:67], 0
	v_mov_b64_e32 v[68:69], 0
	v_mov_b64_e32 v[70:71], 0
	v_mov_b64_e32 v[72:73], 0
	v_mov_b64_e32 v[74:75], 0
	v_mov_b64_e32 v[76:77], 0
	v_mov_b64_e32 v[78:79], 0
	v_mov_b64_e32 v[80:81], 0
	v_mov_b64_e32 v[82:83], 0
	v_mov_b64_e32 v[84:85], 0
	v_mov_b64_e32 v[86:87], 0
	v_mov_b64_e32 v[88:89], 0
	v_mov_b64_e32 v[90:91], 0
	v_mov_b64_e32 v[92:93], 0
	v_mov_b64_e32 v[94:95], 0
	v_mov_b64_e32 v[96:97], 0
	v_mov_b64_e32 v[98:99], 0
	v_mov_b64_e32 v[100:101], 0
	v_mov_b64_e32 v[102:103], 0
	v_mov_b64_e32 v[104:105], 0
	v_mov_b64_e32 v[106:107], 0
	v_mov_b64_e32 v[108:109], 0
	v_mov_b64_e32 v[110:111], 0
	v_mov_b64_e32 v[112:113], 0
	v_mov_b64_e32 v[114:115], 0
	v_mov_b64_e32 v[116:117], 0
	v_mov_b64_e32 v[118:119], 0
	v_mov_b64_e32 v[120:121], 0
	v_mov_b64_e32 v[130:131], 0
	v_mov_b64_e32 v[132:133], 0
	v_mov_b64_e32 v[134:135], 0
	v_mov_b64_e32 v[136:137], 0
	s_waitcnt lgkmcnt(0)
	s_branch .LBB0_2079
	.p2align	6

.LBB0_2500:
	s_ashr_i32 s21, s20, 31
	s_lshl_b64 s[22:23], s[20:21], 19
	v_readlane_b32 s24, v254, 49
	v_readlane_b32 s25, v254, 50
	s_add_u32 s22, s24, s22
	s_addc_u32 s23, s25, s23
	s_and_b64 s[24:25], s[26:27], exec
	s_cselect_b32 s2, s23, s1
	s_cselect_b32 s21, s22, s0
	s_ashr_i32 s19, s18, 31
	s_lshl_b64 s[24:25], s[18:19], 19
	s_add_u32 s24, s4, s24
	s_addc_u32 s25, s5, s25
	s_and_b64 s[40:41], s[26:27], exec
	s_cselect_b32 s19, s25, s37
	s_cselect_b32 s66, s24, s36
	s_cmp_eq_u32 s38, 0
	s_cselect_b32 s67, -2, 0
	s_add_u32 s69, s36, 0x10000
	s_mov_b32 s68, 0
	s_addc_u32 s70, s37, 0
	v_lshl_add_u64 v[210:211], s[0:1], 0, v[204:205]
	v_lshl_add_u64 v[212:213], s[0:1], 0, v[206:207]
	v_mov_b64_e32 v[2:3], 0
	v_mov_b64_e32 v[4:5], 0
	v_mov_b64_e32 v[6:7], 0
	v_mov_b64_e32 v[8:9], 0
	v_mov_b64_e32 v[10:11], 0
	v_mov_b64_e32 v[12:13], 0
	v_mov_b64_e32 v[14:15], 0
	v_mov_b64_e32 v[16:17], 0
	v_mov_b64_e32 v[18:19], 0
	v_mov_b64_e32 v[20:21], 0
	v_mov_b64_e32 v[22:23], 0
	v_mov_b64_e32 v[24:25], 0
	v_mov_b64_e32 v[26:27], 0
	v_mov_b64_e32 v[28:29], 0
	v_mov_b64_e32 v[30:31], 0
	v_mov_b64_e32 v[32:33], 0
	v_mov_b64_e32 v[34:35], 0
	v_mov_b64_e32 v[36:37], 0
	v_mov_b64_e32 v[38:39], 0
	v_mov_b64_e32 v[40:41], 0
	v_mov_b64_e32 v[42:43], 0
	v_mov_b64_e32 v[44:45], 0
	v_mov_b64_e32 v[46:47], 0
	v_mov_b64_e32 v[48:49], 0
	v_mov_b64_e32 v[50:51], 0
	v_mov_b64_e32 v[52:53], 0
	v_mov_b64_e32 v[54:55], 0
	v_mov_b64_e32 v[56:57], 0
	v_mov_b64_e32 v[58:59], 0
	v_mov_b64_e32 v[60:61], 0
	v_mov_b64_e32 v[62:63], 0
	v_mov_b64_e32 v[64:65], 0
	v_mov_b64_e32 v[66:67], 0
	v_mov_b64_e32 v[68:69], 0
	v_mov_b64_e32 v[70:71], 0
	v_mov_b64_e32 v[72:73], 0
	v_mov_b64_e32 v[74:75], 0
	v_mov_b64_e32 v[76:77], 0
	v_mov_b64_e32 v[78:79], 0
	v_mov_b64_e32 v[80:81], 0
	v_mov_b64_e32 v[82:83], 0
	v_mov_b64_e32 v[84:85], 0
	v_mov_b64_e32 v[86:87], 0
	v_mov_b64_e32 v[88:89], 0
	v_mov_b64_e32 v[90:91], 0
	v_mov_b64_e32 v[92:93], 0
	v_mov_b64_e32 v[94:95], 0
	v_mov_b64_e32 v[96:97], 0
	v_mov_b64_e32 v[98:99], 0
	v_mov_b64_e32 v[100:101], 0
	v_mov_b64_e32 v[102:103], 0
	v_mov_b64_e32 v[104:105], 0
	v_mov_b64_e32 v[106:107], 0
	v_mov_b64_e32 v[108:109], 0
	v_mov_b64_e32 v[110:111], 0
	v_mov_b64_e32 v[112:113], 0
	v_mov_b64_e32 v[114:115], 0
	v_mov_b64_e32 v[116:117], 0
	v_mov_b64_e32 v[118:119], 0
	v_mov_b64_e32 v[120:121], 0
	v_mov_b64_e32 v[130:131], 0
	v_mov_b64_e32 v[132:133], 0
	v_mov_b64_e32 v[134:135], 0
	v_mov_b64_e32 v[136:137], 0
	s_branch .LBB0_2502
	.p2align	6

.LBB0_3525:
	s_ashr_i32 s21, s20, 31
	s_lshl_b64 s[22:23], s[20:21], 19
	s_add_u32 s22, s33, s22
	s_addc_u32 s23, s42, s23
	s_and_b64 s[24:25], s[0:1], exec
	s_cselect_b32 s21, s23, s29
	s_cselect_b32 s64, s22, s28
	s_ashr_i32 s19, s18, 31
	s_lshl_b64 s[24:25], s[18:19], 19
	s_add_u32 s24, s43, s24
	s_addc_u32 s25, s44, s25
	s_and_b64 s[36:37], s[0:1], exec
	s_cselect_b32 s19, s25, s31
	s_cselect_b32 s65, s24, s30
	s_cmp_eq_u32 s34, 0
	s_cselect_b32 s66, -2, 0
	s_add_u32 s68, s30, 0x10000
	v_mov_b32_e32 v66, 0
	s_mov_b32 s67, 0
	s_addc_u32 s69, s31, 0
	v_lshl_add_u64 v[210:211], s[28:29], 0, v[202:203]
	v_lshl_add_u64 v[212:213], s[28:29], 0, v[204:205]
	s_mov_b64 s[30:31], 0
	v_mov_b32_e32 v67, 0
	v_mov_b64_e32 v[68:69], 0
	v_mov_b64_e32 v[70:71], 0
	v_mov_b64_e32 v[72:73], 0
	v_mov_b64_e32 v[74:75], 0
	v_mov_b64_e32 v[76:77], 0
	s_waitcnt lgkmcnt(0)
	v_mov_b64_e32 v[78:79], 0
	v_mov_b64_e32 v[80:81], 0
	v_mov_b64_e32 v[82:83], 0
	v_mov_b64_e32 v[84:85], 0
	v_mov_b64_e32 v[86:87], 0
	v_mov_b64_e32 v[88:89], 0
	v_mov_b64_e32 v[90:91], 0
	v_mov_b64_e32 v[92:93], 0
	v_mov_b64_e32 v[94:95], 0
	v_mov_b64_e32 v[96:97], 0
	v_mov_b64_e32 v[98:99], 0
	v_mov_b64_e32 v[100:101], 0
	v_mov_b64_e32 v[102:103], 0
	v_mov_b64_e32 v[104:105], 0
	v_mov_b64_e32 v[106:107], 0
	v_mov_b64_e32 v[108:109], 0
	v_mov_b64_e32 v[110:111], 0
	v_mov_b64_e32 v[112:113], 0
	v_mov_b64_e32 v[114:115], 0
	v_mov_b64_e32 v[116:117], 0
	v_mov_b64_e32 v[118:119], 0
	v_mov_b64_e32 v[120:121], 0
	v_mov_b64_e32 v[122:123], 0
	v_mov_b64_e32 v[124:125], 0
	v_mov_b64_e32 v[126:127], 0
	v_mov_b64_e32 v[128:129], 0
	v_mov_b64_e32 v[130:131], 0
	v_mov_b64_e32 v[132:133], 0
	v_mov_b64_e32 v[134:135], 0
	v_mov_b64_e32 v[136:137], 0
	v_mov_b64_e32 v[138:139], 0
	v_mov_b64_e32 v[140:141], 0
	v_mov_b64_e32 v[142:143], 0
	v_mov_b64_e32 v[144:145], 0
	v_mov_b64_e32 v[146:147], 0
	v_mov_b64_e32 v[148:149], 0
	v_mov_b64_e32 v[150:151], 0
	v_mov_b64_e32 v[152:153], 0
	v_mov_b64_e32 v[154:155], 0
	v_mov_b64_e32 v[156:157], 0
	v_mov_b64_e32 v[158:159], 0
	v_mov_b64_e32 v[160:161], 0
	v_mov_b64_e32 v[162:163], 0
	v_mov_b64_e32 v[164:165], 0
	v_mov_b64_e32 v[166:167], 0
	v_mov_b64_e32 v[168:169], 0
	v_mov_b64_e32 v[170:171], 0
	v_mov_b64_e32 v[172:173], 0
	v_mov_b64_e32 v[174:175], 0
	v_mov_b64_e32 v[176:177], 0
	v_mov_b64_e32 v[178:179], 0
	v_mov_b64_e32 v[180:181], 0
	v_mov_b64_e32 v[182:183], 0
	v_mov_b64_e32 v[184:185], 0
	v_mov_b64_e32 v[186:187], 0
	v_mov_b64_e32 v[188:189], 0
	v_mov_b64_e32 v[190:191], 0
	v_mov_b64_e32 v[192:193], 0
	s_branch .LBB0_3527
	.p2align	6

.Lp15_rs:
	s_branch .LBB0_3831
	.p2align	6

.LBB0_3924:
	s_cmp_eq_u32 s30, 0
	s_cselect_b32 s71, -2, 0
	s_add_u32 s73, s28, 0x10000
	v_mov_b32_e32 v66, 0
	s_mov_b32 s72, 0
	s_addc_u32 s74, s29, 0
	v_lshl_add_u64 v[210:211], s[26:27], 0, v[202:203]
	v_lshl_add_u64 v[212:213], s[26:27], 0, v[204:205]
	s_mov_b64 s[28:29], 0
	v_mov_b32_e32 v67, 0
	v_mov_b64_e32 v[68:69], 0
	v_mov_b64_e32 v[70:71], 0
	v_mov_b64_e32 v[72:73], 0
	v_mov_b64_e32 v[74:75], 0
	v_mov_b64_e32 v[76:77], 0
	v_mov_b64_e32 v[78:79], 0
	v_mov_b64_e32 v[80:81], 0
	v_mov_b64_e32 v[82:83], 0
	v_mov_b64_e32 v[84:85], 0
	v_mov_b64_e32 v[86:87], 0
	v_mov_b64_e32 v[88:89], 0
	v_mov_b64_e32 v[90:91], 0
	v_mov_b64_e32 v[92:93], 0
	v_mov_b64_e32 v[94:95], 0
	v_mov_b64_e32 v[96:97], 0
	v_mov_b64_e32 v[98:99], 0
	v_mov_b64_e32 v[100:101], 0
	v_mov_b64_e32 v[102:103], 0
	v_mov_b64_e32 v[104:105], 0
	v_mov_b64_e32 v[106:107], 0
	v_mov_b64_e32 v[108:109], 0
	v_mov_b64_e32 v[110:111], 0
	v_mov_b64_e32 v[112:113], 0
	v_mov_b64_e32 v[114:115], 0
	v_mov_b64_e32 v[116:117], 0
	v_mov_b64_e32 v[118:119], 0
	v_mov_b64_e32 v[120:121], 0
	v_mov_b64_e32 v[122:123], 0
	v_mov_b64_e32 v[124:125], 0
	v_mov_b64_e32 v[126:127], 0
	v_mov_b64_e32 v[128:129], 0
	v_mov_b64_e32 v[130:131], 0
	v_mov_b64_e32 v[132:133], 0
	v_mov_b64_e32 v[134:135], 0
	v_mov_b64_e32 v[136:137], 0
	v_mov_b64_e32 v[138:139], 0
	v_mov_b64_e32 v[140:141], 0
	v_mov_b64_e32 v[142:143], 0
	v_mov_b64_e32 v[144:145], 0
	v_mov_b64_e32 v[146:147], 0
	v_mov_b64_e32 v[148:149], 0
	v_mov_b64_e32 v[150:151], 0
	v_mov_b64_e32 v[152:153], 0
	v_mov_b64_e32 v[154:155], 0
	v_mov_b64_e32 v[156:157], 0
	v_mov_b64_e32 v[158:159], 0
	v_mov_b64_e32 v[160:161], 0
	v_mov_b64_e32 v[162:163], 0
	v_mov_b64_e32 v[164:165], 0
	v_mov_b64_e32 v[166:167], 0
	v_mov_b64_e32 v[168:169], 0
	v_mov_b64_e32 v[170:171], 0
	v_mov_b64_e32 v[172:173], 0
	v_mov_b64_e32 v[174:175], 0
	v_mov_b64_e32 v[176:177], 0
	v_mov_b64_e32 v[178:179], 0
	v_mov_b64_e32 v[180:181], 0
	v_mov_b64_e32 v[182:183], 0
	v_mov_b64_e32 v[184:185], 0
	v_mov_b64_e32 v[186:187], 0
	v_mov_b64_e32 v[188:189], 0
	v_mov_b64_e32 v[190:191], 0
	v_mov_b64_e32 v[192:193], 0
	s_branch .LBB0_3926
	.p2align	6

.LBB0_3947:
	s_lshl_b32 s8, s8, 5
	s_and_b32 s26, s8, 0x60
	v_lshl_or_b32 v3, s9, 13, v219
	v_lshlrev_b32_e32 v4, 1, v248
	s_lshr_b32 s8, s26, 3
	v_lshlrev_b32_e32 v2, 6, v248
	v_and_b32_e32 v4, 16, v4
	v_or_b32_e32 v5, v3, v218
	v_or_b32_e32 v6, s8, v215
	s_add_u32 s8, s0, 0x8000
	v_lshl_or_b32 v202, s9, 6, v248
	v_or3_b32 v5, v5, v2, v4
	v_bitop3_b32 v2, v2, v4, v217 bitop3:0x36
	s_addc_u32 s9, s1, 0
	v_or_b32_e32 v4, v2, v3
	s_add_i32 m0, s20, 0x18000
	v_lshl_add_u64 v[2:3], s[8:9], 0, v[196:197]
	s_waitcnt vmcnt(2)
	s_barrier
	global_load_lds_dwordx4 v[2:3], off
	s_add_i32 m0, s20, 0x1a000
	v_lshl_add_u64 v[2:3], s[8:9], 0, v[200:201]
	s_add_u32 s8, s4, 0x8000
	s_addc_u32 s9, s5, 0
	s_add_i32 s30, s20, 0x8000
	global_load_lds_dwordx4 v[2:3], off
	v_lshl_add_u64 v[2:3], s[8:9], 0, v[194:195]
	s_mov_b32 m0, s30
	s_add_i32 s31, s20, 0xa000
	global_load_lds_dwordx4 v[2:3], off
	v_lshl_add_u64 v[2:3], s[8:9], 0, v[198:199]
	s_add_u32 s8, s0, 0x9000
	s_mov_b32 m0, s31
	s_addc_u32 s9, s1, 0
	global_load_lds_dwordx4 v[2:3], off
	s_add_i32 m0, s20, 0x1c000
	v_lshl_add_u64 v[2:3], s[8:9], 0, v[196:197]
	global_load_lds_dwordx4 v[2:3], off
	v_lshl_add_u64 v[2:3], s[8:9], 0, v[200:201]
	s_add_i32 m0, s20, 0x1e000
	s_mul_hi_i32 s8, s10, 0x1c0000
	global_load_lds_dwordx4 v[2:3], off
	s_mul_i32 s10, s10, 0x1c0000
	v_lshlrev_b32_e32 v3, 12, v0
	v_lshlrev_b32_e32 v6, 10, v6
	s_add_u32 s6, s10, s6
	v_lshlrev_b32_e32 v2, 8, v0
	v_and_b32_e32 v3, 0x2000, v3
	v_or_b32_e32 v203, v216, v6
	v_or_b32_e32 v208, v6, v220
	s_addc_u32 s7, s8, s7
	v_and_or_b32 v6, v2, s12, v3
	s_movk_i32 s8, 0x600
	v_lshlrev_b32_e32 v2, 2, v0
	v_bfe_u32 v3, v0, 2, 4
	v_and_or_b32 v2, v2, s8, v6
	v_lshlrev_b32_e32 v7, 5, v3
	s_add_u32 s6, s96, s6
	v_or3_b32 v2, v2, v7, v1
	v_mov_b32_e32 v3, v197
	s_addc_u32 s7, s97, s7
	v_lshl_add_u64 v[204:205], s[6:7], 0, v[2:3]
	v_lshrrev_b32_e32 v2, 2, v214
	s_movk_i32 s8, 0xe00
	s_waitcnt vmcnt(6)
	v_and_or_b32 v2, v2, s8, v6
	s_add_i32 s8, 0, 0x10000
	s_add_i32 s38, 0, 0x18000
	s_add_i32 s39, 0, 0x1c000
	v_or3_b32 v2, v2, v7, v1
	v_add_u32_e32 v1, s8, v203
	v_add_u32_e32 v209, s8, v208
	s_add_i32 s8, 0, 0x14000
	s_add_i32 s40, s38, s11
	s_add_i32 s42, s39, s11
	s_mov_b32 s34, -2
	v_lshl_add_u64 v[206:207], s[6:7], 0, v[2:3]
	s_lshl_b32 s35, s19, 15
	s_mov_b64 s[6:7], 0x10000
	v_add_u32_e32 v210, s8, v203
	v_add_u32_e32 v211, s8, v208
	v_add_u32_e32 v212, 0, v5
	v_add_u32_e32 v213, 0, v4
	s_mov_b64 s[8:9], 0x551f9000
	s_add_i32 s36, s20, 0xc000
	s_add_i32 s37, s20, 0xe000
	v_mov_b32_e32 v214, 0x7f7f7f7f
	s_add_i32 s41, s40, 0x2000
	s_add_i32 s43, s42, 0x2000
	v_mov_b64_e32 v[66:67], 0
	v_mov_b64_e32 v[68:69], 0
	v_mov_b64_e32 v[70:71], 0
	v_mov_b64_e32 v[72:73], 0
	v_mov_b64_e32 v[74:75], 0
	v_mov_b64_e32 v[76:77], 0
	v_mov_b64_e32 v[78:79], 0
	v_mov_b64_e32 v[80:81], 0
	v_mov_b64_e32 v[82:83], 0
	v_mov_b64_e32 v[84:85], 0
	v_mov_b64_e32 v[86:87], 0
	v_mov_b64_e32 v[88:89], 0
	v_mov_b64_e32 v[90:91], 0
	v_mov_b64_e32 v[92:93], 0
	v_mov_b64_e32 v[94:95], 0
	v_mov_b64_e32 v[96:97], 0
	v_mov_b64_e32 v[98:99], 0
	v_mov_b64_e32 v[100:101], 0
	v_mov_b64_e32 v[102:103], 0
	v_mov_b64_e32 v[104:105], 0
	v_mov_b64_e32 v[106:107], 0
	v_mov_b64_e32 v[108:109], 0
	v_mov_b64_e32 v[110:111], 0
	v_mov_b64_e32 v[112:113], 0
	v_mov_b64_e32 v[114:115], 0
	v_mov_b64_e32 v[116:117], 0
	v_mov_b64_e32 v[118:119], 0
	v_mov_b64_e32 v[120:121], 0
	v_mov_b64_e32 v[122:123], 0
	v_mov_b64_e32 v[124:125], 0
	v_mov_b64_e32 v[126:127], 0
	v_mov_b64_e32 v[128:129], 0
	v_mov_b64_e32 v[130:131], 0
	v_mov_b64_e32 v[132:133], 0
	v_mov_b64_e32 v[134:135], 0
	v_mov_b64_e32 v[136:137], 0
	v_mov_b64_e32 v[138:139], 0
	v_mov_b64_e32 v[140:141], 0
	v_mov_b64_e32 v[142:143], 0
	v_mov_b64_e32 v[144:145], 0
	v_mov_b64_e32 v[146:147], 0
	v_mov_b64_e32 v[148:149], 0
	v_mov_b64_e32 v[150:151], 0
	v_mov_b64_e32 v[152:153], 0
	v_mov_b64_e32 v[154:155], 0
	v_mov_b64_e32 v[156:157], 0
	v_mov_b64_e32 v[158:159], 0
	v_mov_b64_e32 v[160:161], 0
	v_mov_b64_e32 v[162:163], 0
	v_mov_b64_e32 v[164:165], 0
	v_mov_b64_e32 v[166:167], 0
	v_mov_b64_e32 v[168:169], 0
	v_mov_b64_e32 v[170:171], 0
	v_mov_b64_e32 v[172:173], 0
	v_mov_b64_e32 v[174:175], 0
	v_mov_b64_e32 v[176:177], 0
	v_mov_b64_e32 v[178:179], 0
	v_mov_b64_e32 v[180:181], 0
	v_mov_b64_e32 v[182:183], 0
	v_mov_b64_e32 v[184:185], 0
	v_mov_b64_e32 v[186:187], 0
	v_mov_b64_e32 v[188:189], 0
	v_mov_b64_e32 v[190:191], 0
	v_mov_b64_e32 v[192:193], 0
	s_barrier
	s_branch .LBB0_3949
	.p2align	6
